# attention sub-tiles: deferred-max test branches on vccz of the inverted compare (one scalar compare less on the dependent chain)
# baseline (speedup 1.0000x reference)
.LBB0_452:
	s_nop 0
	v_max3_f32 v2, v70, v71, v72
	v_max3_f32 v4, v73, v74, v75
	v_max3_f32 v5, v76, v77, v78
	v_max3_f32 v175, v79, v80, v81
	v_max3_f32 v2, v2, v4, v5
	v_max3_f32 v4, v82, v83, v84
	v_max3_f32 v2, v2, v175, v4
	v_max_f32_e32 v2, v2, v85
	v_sub_f32_e32 v4, v2, v168
	v_cmp_nge_f32_e32 vcc, s76, v4
	s_cbranch_vccz .LBB0_454
	v_mov_b32_e32 v4, v2
	s_nop 1
	v_permlane32_swap_b32_e32 v2, v4
	v_max_f32_e32 v2, v2, v4
	v_max_f32_e32 v2, v2, v2
	v_max_f32_e32 v4, v168, v168
	v_max_f32_e32 v4, v4, v2
	v_sub_f32_e32 v2, v168, v4
	v_mul_f32_e32 v2, 0x3fb8aa3b, v2
	v_exp_f32_e32 v2, v2
	v_mov_b32_e32 v168, v4
	v_mul_f32_e32 v167, v167, v2
	v_pk_mul_f32 v[68:69], v[68:69], v[2:3] op_sel_hi:[1,0]
	v_pk_mul_f32 v[66:67], v[66:67], v[2:3] op_sel_hi:[1,0]
	v_pk_mul_f32 v[64:65], v[64:65], v[2:3] op_sel_hi:[1,0]
	v_pk_mul_f32 v[62:63], v[62:63], v[2:3] op_sel_hi:[1,0]
	v_pk_mul_f32 v[60:61], v[60:61], v[2:3] op_sel_hi:[1,0]
	v_pk_mul_f32 v[58:59], v[58:59], v[2:3] op_sel_hi:[1,0]
	v_pk_mul_f32 v[56:57], v[56:57], v[2:3] op_sel_hi:[1,0]
	v_pk_mul_f32 v[54:55], v[54:55], v[2:3] op_sel_hi:[1,0]
	v_pk_mul_f32 v[52:53], v[52:53], v[2:3] op_sel_hi:[1,0]
	v_pk_mul_f32 v[50:51], v[50:51], v[2:3] op_sel_hi:[1,0]
	v_pk_mul_f32 v[48:49], v[48:49], v[2:3] op_sel_hi:[1,0]
	v_pk_mul_f32 v[46:47], v[46:47], v[2:3] op_sel_hi:[1,0]
	v_pk_mul_f32 v[44:45], v[44:45], v[2:3] op_sel_hi:[1,0]
	v_pk_mul_f32 v[42:43], v[42:43], v[2:3] op_sel_hi:[1,0]
	v_pk_mul_f32 v[40:41], v[40:41], v[2:3] op_sel_hi:[1,0]
	v_pk_mul_f32 v[38:39], v[38:39], v[2:3] op_sel_hi:[1,0]
	v_pk_mul_f32 v[36:37], v[36:37], v[2:3] op_sel_hi:[1,0]
	v_pk_mul_f32 v[34:35], v[34:35], v[2:3] op_sel_hi:[1,0]
	v_pk_mul_f32 v[32:33], v[32:33], v[2:3] op_sel_hi:[1,0]
	v_pk_mul_f32 v[30:31], v[30:31], v[2:3] op_sel_hi:[1,0]
	v_pk_mul_f32 v[28:29], v[28:29], v[2:3] op_sel_hi:[1,0]
	v_pk_mul_f32 v[26:27], v[26:27], v[2:3] op_sel_hi:[1,0]
	v_pk_mul_f32 v[24:25], v[24:25], v[2:3] op_sel_hi:[1,0]
	v_pk_mul_f32 v[22:23], v[22:23], v[2:3] op_sel_hi:[1,0]
	v_pk_mul_f32 v[20:21], v[20:21], v[2:3] op_sel_hi:[1,0]
	v_pk_mul_f32 v[18:19], v[18:19], v[2:3] op_sel_hi:[1,0]
	v_pk_mul_f32 v[16:17], v[16:17], v[2:3] op_sel_hi:[1,0]
	v_pk_mul_f32 v[14:15], v[14:15], v[2:3] op_sel_hi:[1,0]
	v_pk_mul_f32 v[12:13], v[12:13], v[2:3] op_sel_hi:[1,0]
	v_pk_mul_f32 v[10:11], v[10:11], v[2:3] op_sel_hi:[1,0]
	v_pk_mul_f32 v[8:9], v[8:9], v[2:3] op_sel_hi:[1,0]
	v_pk_mul_f32 v[6:7], v[6:7], v[2:3] op_sel_hi:[1,0]

.LBB0_458:
	s_nop 0
	v_max3_f32 v2, v70, v71, v72
	v_max3_f32 v4, v73, v74, v75
	v_max3_f32 v5, v76, v77, v78
	v_max3_f32 v169, v79, v80, v81
	v_max3_f32 v2, v2, v4, v5
	v_max3_f32 v4, v82, v83, v84
	v_max3_f32 v2, v2, v169, v4
	v_max_f32_e32 v2, v2, v85
	v_sub_f32_e32 v4, v2, v168
	v_cmp_nge_f32_e32 vcc, s76, v4
	s_cbranch_vccz .LBB0_460
	v_mov_b32_e32 v4, v2
	s_nop 1
	v_permlane32_swap_b32_e32 v2, v4
	v_max_f32_e32 v2, v2, v4
	v_max_f32_e32 v2, v2, v2
	v_max_f32_e32 v4, v168, v168
	v_max_f32_e32 v4, v4, v2
	v_sub_f32_e32 v2, v168, v4
	v_mul_f32_e32 v2, 0x3fb8aa3b, v2
	v_exp_f32_e32 v2, v2
	v_mov_b32_e32 v168, v4
	v_mul_f32_e32 v167, v167, v2
	v_pk_mul_f32 v[68:69], v[68:69], v[2:3] op_sel_hi:[1,0]
	v_pk_mul_f32 v[66:67], v[66:67], v[2:3] op_sel_hi:[1,0]
	v_pk_mul_f32 v[64:65], v[64:65], v[2:3] op_sel_hi:[1,0]
	v_pk_mul_f32 v[62:63], v[62:63], v[2:3] op_sel_hi:[1,0]
	v_pk_mul_f32 v[60:61], v[60:61], v[2:3] op_sel_hi:[1,0]
	v_pk_mul_f32 v[58:59], v[58:59], v[2:3] op_sel_hi:[1,0]
	v_pk_mul_f32 v[56:57], v[56:57], v[2:3] op_sel_hi:[1,0]
	v_pk_mul_f32 v[54:55], v[54:55], v[2:3] op_sel_hi:[1,0]
	v_pk_mul_f32 v[52:53], v[52:53], v[2:3] op_sel_hi:[1,0]
	v_pk_mul_f32 v[50:51], v[50:51], v[2:3] op_sel_hi:[1,0]
	v_pk_mul_f32 v[48:49], v[48:49], v[2:3] op_sel_hi:[1,0]
	v_pk_mul_f32 v[46:47], v[46:47], v[2:3] op_sel_hi:[1,0]
	v_pk_mul_f32 v[44:45], v[44:45], v[2:3] op_sel_hi:[1,0]
	v_pk_mul_f32 v[42:43], v[42:43], v[2:3] op_sel_hi:[1,0]
	v_pk_mul_f32 v[40:41], v[40:41], v[2:3] op_sel_hi:[1,0]
	v_pk_mul_f32 v[38:39], v[38:39], v[2:3] op_sel_hi:[1,0]
	v_pk_mul_f32 v[36:37], v[36:37], v[2:3] op_sel_hi:[1,0]
	v_pk_mul_f32 v[34:35], v[34:35], v[2:3] op_sel_hi:[1,0]
	v_pk_mul_f32 v[32:33], v[32:33], v[2:3] op_sel_hi:[1,0]
	v_pk_mul_f32 v[30:31], v[30:31], v[2:3] op_sel_hi:[1,0]
	v_pk_mul_f32 v[28:29], v[28:29], v[2:3] op_sel_hi:[1,0]
	v_pk_mul_f32 v[26:27], v[26:27], v[2:3] op_sel_hi:[1,0]
	v_pk_mul_f32 v[24:25], v[24:25], v[2:3] op_sel_hi:[1,0]
	v_pk_mul_f32 v[22:23], v[22:23], v[2:3] op_sel_hi:[1,0]
	v_pk_mul_f32 v[20:21], v[20:21], v[2:3] op_sel_hi:[1,0]
	v_pk_mul_f32 v[18:19], v[18:19], v[2:3] op_sel_hi:[1,0]
	v_pk_mul_f32 v[16:17], v[16:17], v[2:3] op_sel_hi:[1,0]
	v_pk_mul_f32 v[14:15], v[14:15], v[2:3] op_sel_hi:[1,0]
	v_pk_mul_f32 v[12:13], v[12:13], v[2:3] op_sel_hi:[1,0]
	v_pk_mul_f32 v[10:11], v[10:11], v[2:3] op_sel_hi:[1,0]
	v_pk_mul_f32 v[8:9], v[8:9], v[2:3] op_sel_hi:[1,0]
	v_pk_mul_f32 v[6:7], v[6:7], v[2:3] op_sel_hi:[1,0]

.LBB0_524:
	s_nop 1
	v_max3_f32 v2, v50, v51, v52
	v_max3_f32 v116, v53, v54, v55
	v_max3_f32 v117, v56, v57, v58
	v_max3_f32 v118, v59, v60, v61
	v_max3_f32 v2, v2, v116, v117
	v_max3_f32 v116, v62, v63, v64
	v_max3_f32 v2, v2, v118, v116
	v_max_f32_e32 v2, v2, v65
	v_sub_f32_e32 v116, v2, v110
	v_cmp_nge_f32_e32 vcc, s76, v116
	s_cbranch_vccz .LBB0_526
	v_mov_b32_e32 v116, v2
	s_nop 1
	v_permlane32_swap_b32_e32 v2, v116
	v_max_f32_e32 v2, v2, v116
	v_max_f32_e32 v2, v2, v2
	v_max_f32_e32 v116, v110, v110
	v_max_f32_e32 v116, v116, v2
	v_sub_f32_e32 v2, v110, v116
	v_mul_f32_e32 v2, 0x3fb8aa3b, v2
	v_exp_f32_e32 v2, v2
	v_mov_b32_e32 v110, v116
	v_mul_f32_e32 v107, v107, v2
	v_pk_mul_f32 v[48:49], v[48:49], v[2:3] op_sel_hi:[1,0]
	v_pk_mul_f32 v[46:47], v[46:47], v[2:3] op_sel_hi:[1,0]
	v_pk_mul_f32 v[44:45], v[44:45], v[2:3] op_sel_hi:[1,0]
	v_pk_mul_f32 v[42:43], v[42:43], v[2:3] op_sel_hi:[1,0]
	v_pk_mul_f32 v[40:41], v[40:41], v[2:3] op_sel_hi:[1,0]
	v_pk_mul_f32 v[38:39], v[38:39], v[2:3] op_sel_hi:[1,0]
	v_pk_mul_f32 v[36:37], v[36:37], v[2:3] op_sel_hi:[1,0]
	v_pk_mul_f32 v[34:35], v[34:35], v[2:3] op_sel_hi:[1,0]
	v_pk_mul_f32 v[32:33], v[32:33], v[2:3] op_sel_hi:[1,0]
	v_pk_mul_f32 v[30:31], v[30:31], v[2:3] op_sel_hi:[1,0]
	v_pk_mul_f32 v[28:29], v[28:29], v[2:3] op_sel_hi:[1,0]
	v_pk_mul_f32 v[26:27], v[26:27], v[2:3] op_sel_hi:[1,0]
	v_pk_mul_f32 v[24:25], v[24:25], v[2:3] op_sel_hi:[1,0]
	v_pk_mul_f32 v[22:23], v[22:23], v[2:3] op_sel_hi:[1,0]
	v_pk_mul_f32 v[20:21], v[20:21], v[2:3] op_sel_hi:[1,0]
	v_pk_mul_f32 v[18:19], v[18:19], v[2:3] op_sel_hi:[1,0]

.LBB0_530:
	s_nop 0
	v_max3_f32 v2, v50, v51, v52
	v_max3_f32 v16, v53, v54, v55
	v_max3_f32 v17, v56, v57, v58
	v_max3_f32 v111, v59, v60, v61
	v_max3_f32 v2, v2, v16, v17
	v_max3_f32 v16, v62, v63, v64
	v_max3_f32 v2, v2, v111, v16
	v_max_f32_e32 v2, v2, v65
	v_sub_f32_e32 v16, v2, v110
	v_cmp_nge_f32_e32 vcc, s76, v16
	s_cbranch_vccz .LBB0_509
	v_mov_b32_e32 v16, v2
	s_nop 1
	v_permlane32_swap_b32_e32 v2, v16
	v_max_f32_e32 v2, v2, v16
	v_max_f32_e32 v2, v2, v2
	v_max_f32_e32 v16, v110, v110
	v_max_f32_e32 v16, v16, v2
	v_sub_f32_e32 v2, v110, v16
	v_mul_f32_e32 v2, 0x3fb8aa3b, v2
	v_exp_f32_e32 v2, v2
	v_mov_b32_e32 v110, v16
	v_mul_f32_e32 v107, v107, v2
	v_pk_mul_f32 v[48:49], v[48:49], v[2:3] op_sel_hi:[1,0]
	v_pk_mul_f32 v[46:47], v[46:47], v[2:3] op_sel_hi:[1,0]
	v_pk_mul_f32 v[44:45], v[44:45], v[2:3] op_sel_hi:[1,0]
	v_pk_mul_f32 v[42:43], v[42:43], v[2:3] op_sel_hi:[1,0]
	v_pk_mul_f32 v[40:41], v[40:41], v[2:3] op_sel_hi:[1,0]
	v_pk_mul_f32 v[38:39], v[38:39], v[2:3] op_sel_hi:[1,0]
	v_pk_mul_f32 v[36:37], v[36:37], v[2:3] op_sel_hi:[1,0]
	v_pk_mul_f32 v[34:35], v[34:35], v[2:3] op_sel_hi:[1,0]
	v_pk_mul_f32 v[32:33], v[32:33], v[2:3] op_sel_hi:[1,0]
	v_pk_mul_f32 v[30:31], v[30:31], v[2:3] op_sel_hi:[1,0]
	v_pk_mul_f32 v[28:29], v[28:29], v[2:3] op_sel_hi:[1,0]
	v_pk_mul_f32 v[26:27], v[26:27], v[2:3] op_sel_hi:[1,0]
	v_pk_mul_f32 v[24:25], v[24:25], v[2:3] op_sel_hi:[1,0]
	v_pk_mul_f32 v[22:23], v[22:23], v[2:3] op_sel_hi:[1,0]
	v_pk_mul_f32 v[20:21], v[20:21], v[2:3] op_sel_hi:[1,0]
	v_pk_mul_f32 v[18:19], v[18:19], v[2:3] op_sel_hi:[1,0]
	s_branch .LBB0_509

.LBB0_687:
	s_nop 0
	v_max3_f32 v2, v82, v83, v84
	v_max3_f32 v164, v85, v86, v87
	v_max3_f32 v165, v88, v89, v90
	v_max3_f32 v166, v91, v92, v93
	v_max3_f32 v2, v2, v164, v165
	v_max3_f32 v164, v94, v95, v96
	v_max3_f32 v2, v2, v166, v164
	v_max_f32_e32 v2, v2, v97
	v_sub_f32_e32 v164, v2, v158
	v_cmp_nge_f32_e32 vcc, s76, v164
	s_cbranch_vccz .LBB0_689
	v_mov_b32_e32 v164, v2
	s_nop 1
	v_permlane32_swap_b32_e32 v2, v164
	v_max_f32_e32 v2, v2, v164
	v_max_f32_e32 v2, v2, v2
	v_max_f32_e32 v164, v158, v158
	v_max_f32_e32 v164, v164, v2
	v_sub_f32_e32 v2, v158, v164
	v_mul_f32_e32 v2, 0x3fb8aa3b, v2
	v_exp_f32_e32 v2, v2
	v_mov_b32_e32 v158, v164
	v_mul_f32_e32 v144, v144, v2
	v_pk_mul_f32 v[80:81], v[80:81], v[2:3] op_sel_hi:[1,0]
	v_pk_mul_f32 v[78:79], v[78:79], v[2:3] op_sel_hi:[1,0]
	v_pk_mul_f32 v[76:77], v[76:77], v[2:3] op_sel_hi:[1,0]
	v_pk_mul_f32 v[74:75], v[74:75], v[2:3] op_sel_hi:[1,0]
	v_pk_mul_f32 v[72:73], v[72:73], v[2:3] op_sel_hi:[1,0]
	v_pk_mul_f32 v[70:71], v[70:71], v[2:3] op_sel_hi:[1,0]
	v_pk_mul_f32 v[68:69], v[68:69], v[2:3] op_sel_hi:[1,0]
	v_pk_mul_f32 v[66:67], v[66:67], v[2:3] op_sel_hi:[1,0]
	v_pk_mul_f32 v[64:65], v[64:65], v[2:3] op_sel_hi:[1,0]
	v_pk_mul_f32 v[62:63], v[62:63], v[2:3] op_sel_hi:[1,0]
	v_pk_mul_f32 v[60:61], v[60:61], v[2:3] op_sel_hi:[1,0]
	v_pk_mul_f32 v[58:59], v[58:59], v[2:3] op_sel_hi:[1,0]
	v_pk_mul_f32 v[56:57], v[56:57], v[2:3] op_sel_hi:[1,0]
	v_pk_mul_f32 v[54:55], v[54:55], v[2:3] op_sel_hi:[1,0]
	v_pk_mul_f32 v[52:53], v[52:53], v[2:3] op_sel_hi:[1,0]
	v_pk_mul_f32 v[50:51], v[50:51], v[2:3] op_sel_hi:[1,0]

.LBB0_695:
	s_nop 0
	v_max3_f32 v2, v82, v83, v84
	v_max3_f32 v16, v85, v86, v87
	v_max3_f32 v17, v88, v89, v90
	v_max3_f32 v159, v91, v92, v93
	v_max3_f32 v2, v2, v16, v17
	v_max3_f32 v16, v94, v95, v96
	v_max3_f32 v2, v2, v159, v16
	v_max_f32_e32 v2, v2, v97
	v_sub_f32_e32 v16, v2, v158
	v_cmp_nge_f32_e32 vcc, s76, v16
	s_cbranch_vccz .LBB0_668
	v_mov_b32_e32 v16, v2
	s_nop 1
	v_permlane32_swap_b32_e32 v2, v16
	v_max_f32_e32 v2, v2, v16
	v_max_f32_e32 v2, v2, v2
	v_max_f32_e32 v16, v158, v158
	v_max_f32_e32 v16, v16, v2
	v_sub_f32_e32 v2, v158, v16
	v_mul_f32_e32 v2, 0x3fb8aa3b, v2
	v_exp_f32_e32 v2, v2
	v_mov_b32_e32 v158, v16
	v_mul_f32_e32 v144, v144, v2
	v_pk_mul_f32 v[80:81], v[80:81], v[2:3] op_sel_hi:[1,0]
	v_pk_mul_f32 v[78:79], v[78:79], v[2:3] op_sel_hi:[1,0]
	v_pk_mul_f32 v[76:77], v[76:77], v[2:3] op_sel_hi:[1,0]
	v_pk_mul_f32 v[74:75], v[74:75], v[2:3] op_sel_hi:[1,0]
	v_pk_mul_f32 v[72:73], v[72:73], v[2:3] op_sel_hi:[1,0]
	v_pk_mul_f32 v[70:71], v[70:71], v[2:3] op_sel_hi:[1,0]
	v_pk_mul_f32 v[68:69], v[68:69], v[2:3] op_sel_hi:[1,0]
	v_pk_mul_f32 v[66:67], v[66:67], v[2:3] op_sel_hi:[1,0]
	v_pk_mul_f32 v[64:65], v[64:65], v[2:3] op_sel_hi:[1,0]
	v_pk_mul_f32 v[62:63], v[62:63], v[2:3] op_sel_hi:[1,0]
	v_pk_mul_f32 v[60:61], v[60:61], v[2:3] op_sel_hi:[1,0]
	v_pk_mul_f32 v[58:59], v[58:59], v[2:3] op_sel_hi:[1,0]
	v_pk_mul_f32 v[56:57], v[56:57], v[2:3] op_sel_hi:[1,0]
	v_pk_mul_f32 v[54:55], v[54:55], v[2:3] op_sel_hi:[1,0]
	v_pk_mul_f32 v[52:53], v[52:53], v[2:3] op_sel_hi:[1,0]
	v_pk_mul_f32 v[50:51], v[50:51], v[2:3] op_sel_hi:[1,0]
	s_branch .LBB0_668

.LBB0_785:
	s_nop 1
	v_max3_f32 v2, v50, v51, v52
	v_max3_f32 v119, v53, v54, v55
	v_max3_f32 v120, v56, v57, v58
	v_max3_f32 v121, v59, v60, v61
	v_max3_f32 v2, v2, v119, v120
	v_max3_f32 v119, v62, v63, v64
	v_max3_f32 v2, v2, v121, v119
	v_max_f32_e32 v2, v2, v65
	v_sub_f32_e32 v119, v2, v113
	v_cmp_nge_f32_e32 vcc, s76, v119
	s_cbranch_vccz .LBB0_787
	v_mov_b32_e32 v119, v2
	s_nop 1
	v_permlane32_swap_b32_e32 v2, v119
	v_max_f32_e32 v2, v2, v119
	v_max_f32_e32 v2, v2, v2
	v_max_f32_e32 v119, v113, v113
	v_max_f32_e32 v119, v119, v2
	v_sub_f32_e32 v2, v113, v119
	v_mul_f32_e32 v2, 0x3fb8aa3b, v2
	v_exp_f32_e32 v2, v2
	v_mov_b32_e32 v113, v119
	v_mul_f32_e32 v108, v108, v2
	v_pk_mul_f32 v[48:49], v[48:49], v[2:3] op_sel_hi:[1,0]
	v_pk_mul_f32 v[46:47], v[46:47], v[2:3] op_sel_hi:[1,0]
	v_pk_mul_f32 v[44:45], v[44:45], v[2:3] op_sel_hi:[1,0]
	v_pk_mul_f32 v[42:43], v[42:43], v[2:3] op_sel_hi:[1,0]
	v_pk_mul_f32 v[40:41], v[40:41], v[2:3] op_sel_hi:[1,0]
	v_pk_mul_f32 v[38:39], v[38:39], v[2:3] op_sel_hi:[1,0]
	v_pk_mul_f32 v[36:37], v[36:37], v[2:3] op_sel_hi:[1,0]
	v_pk_mul_f32 v[34:35], v[34:35], v[2:3] op_sel_hi:[1,0]
	v_pk_mul_f32 v[32:33], v[32:33], v[2:3] op_sel_hi:[1,0]
	v_pk_mul_f32 v[30:31], v[30:31], v[2:3] op_sel_hi:[1,0]
	v_pk_mul_f32 v[28:29], v[28:29], v[2:3] op_sel_hi:[1,0]
	v_pk_mul_f32 v[26:27], v[26:27], v[2:3] op_sel_hi:[1,0]
	v_pk_mul_f32 v[24:25], v[24:25], v[2:3] op_sel_hi:[1,0]
	v_pk_mul_f32 v[22:23], v[22:23], v[2:3] op_sel_hi:[1,0]
	v_pk_mul_f32 v[20:21], v[20:21], v[2:3] op_sel_hi:[1,0]
	v_pk_mul_f32 v[18:19], v[18:19], v[2:3] op_sel_hi:[1,0]

.LBB0_791:
	s_nop 0
	v_max3_f32 v2, v50, v51, v52
	v_max3_f32 v16, v53, v54, v55
	v_max3_f32 v17, v56, v57, v58
	v_max3_f32 v114, v59, v60, v61
	v_max3_f32 v2, v2, v16, v17
	v_max3_f32 v16, v62, v63, v64
	v_max3_f32 v2, v2, v114, v16
	v_max_f32_e32 v2, v2, v65
	v_sub_f32_e32 v16, v2, v113
	v_cmp_nge_f32_e32 vcc, s76, v16
	s_cbranch_vccz .LBB0_770
	v_mov_b32_e32 v16, v2
	s_nop 1
	v_permlane32_swap_b32_e32 v2, v16
	v_max_f32_e32 v2, v2, v16
	v_max_f32_e32 v2, v2, v2
	v_max_f32_e32 v16, v113, v113
	v_max_f32_e32 v16, v16, v2
	v_sub_f32_e32 v2, v113, v16
	v_mul_f32_e32 v2, 0x3fb8aa3b, v2
	v_exp_f32_e32 v2, v2
	v_mov_b32_e32 v113, v16
	v_mul_f32_e32 v108, v108, v2
	v_pk_mul_f32 v[48:49], v[48:49], v[2:3] op_sel_hi:[1,0]
	v_pk_mul_f32 v[46:47], v[46:47], v[2:3] op_sel_hi:[1,0]
	v_pk_mul_f32 v[44:45], v[44:45], v[2:3] op_sel_hi:[1,0]
	v_pk_mul_f32 v[42:43], v[42:43], v[2:3] op_sel_hi:[1,0]
	v_pk_mul_f32 v[40:41], v[40:41], v[2:3] op_sel_hi:[1,0]
	v_pk_mul_f32 v[38:39], v[38:39], v[2:3] op_sel_hi:[1,0]
	v_pk_mul_f32 v[36:37], v[36:37], v[2:3] op_sel_hi:[1,0]
	v_pk_mul_f32 v[34:35], v[34:35], v[2:3] op_sel_hi:[1,0]
	v_pk_mul_f32 v[32:33], v[32:33], v[2:3] op_sel_hi:[1,0]
	v_pk_mul_f32 v[30:31], v[30:31], v[2:3] op_sel_hi:[1,0]
	v_pk_mul_f32 v[28:29], v[28:29], v[2:3] op_sel_hi:[1,0]
	v_pk_mul_f32 v[26:27], v[26:27], v[2:3] op_sel_hi:[1,0]
	v_pk_mul_f32 v[24:25], v[24:25], v[2:3] op_sel_hi:[1,0]
	v_pk_mul_f32 v[22:23], v[22:23], v[2:3] op_sel_hi:[1,0]
	v_pk_mul_f32 v[20:21], v[20:21], v[2:3] op_sel_hi:[1,0]
	v_pk_mul_f32 v[18:19], v[18:19], v[2:3] op_sel_hi:[1,0]
	s_branch .LBB0_770
